# speedup vs baseline: 1.1354x; 1.0306x over previous
.LBB0_21:
	v_exp_f32_e64 v156, -|v154|
	v_max_f32 v157, 0, v154
	v_add_f32 v156, 1.0, v156
	v_log_f32 v156, v156
	s_nop 0
	v_fma_mixlo_f16 v155, v156, 1.0, v157
	ds_write_b16 v148, v155
	v_mov_b32_e32 v192, v106
	v_mov_b32_e32 v193, v110
	v_mul_f32 v182, -2.0, v153
	s_nop 5
	ds_read_b128 v[208:211], v139
	s_waitcnt lgkmcnt(1)
	s_barrier
	ds_read_b128 v[212:215], v140
	s_waitcnt lgkmcnt(1)
	v_smfmac_f32_16x16x64_f16 v[192:195], v[208:211], v[6:13], v191
	ds_read_b128 v[216:219], v141
	s_waitcnt lgkmcnt(1)
	v_smfmac_f32_16x16x64_f16 v[192:195], v[212:215], v[14:21], v191
	ds_read_b128 v[220:223], v142
	s_waitcnt lgkmcnt(1)
	v_smfmac_f32_16x16x64_f16 v[192:195], v[216:219], v[26:33], v191
	s_waitcnt lgkmcnt(0)
	v_smfmac_f32_16x16x64_f16 v[192:195], v[220:223], v[34:41], v191
	s_nop 7
	v_cndmask_b32_e64 v154, v192, v193, s[0:1]
	v_exp_f32_e64 v156, -|v154|
	v_max_f32 v157, 0, v154
	v_add_f32 v156, 1.0, v156
	v_log_f32 v156, v156
	s_nop 0
	v_fma_mixlo_f16 v155, v156, 1.0, v157
	ds_write_b16 v149, v155
	v_mov_b32_e32 v200, v114
	v_mov_b32_e32 v201, v118
	v_mov_b32_e32 v204, v122
	v_mov_b32_e32 v205, v126
	s_nop 5
	ds_read_b128 v[208:211], v143
	s_waitcnt lgkmcnt(1)
	s_barrier
	ds_read_b128 v[212:215], v144
	s_waitcnt lgkmcnt(1)
	v_smfmac_f32_16x16x64_f16 v[200:203], v[208:211], v[42:49], v191
	ds_read_b128 v[216:219], v145
	v_smfmac_f32_16x16x64_f16 v[204:207], v[208:211], v[74:81], v191
	ds_read_b128 v[220:223], v146
	s_waitcnt lgkmcnt(2)
	v_smfmac_f32_16x16x64_f16 v[200:203], v[212:215], v[50:57], v191
	v_smfmac_f32_16x16x64_f16 v[204:207], v[212:215], v[82:89], v191
	s_waitcnt lgkmcnt(1)
	v_smfmac_f32_16x16x64_f16 v[200:203], v[216:219], v[58:65], v191
	v_smfmac_f32_16x16x64_f16 v[204:207], v[216:219], v[90:97], v191
	s_waitcnt lgkmcnt(0)
	v_smfmac_f32_16x16x64_f16 v[200:203], v[220:223], v[66:73], v191
	v_smfmac_f32_16x16x64_f16 v[204:207], v[220:223], v[98:105], v191
	s_nop 6
	v_cndmask_b32_e64 v170, v201, v200, s[6:7]
	v_cndmask_b32_e64 v170, v170, v204, s[0:1]
	v_cndmask_b32_e64 v170, v170, v205, s[4:5]
	v_exp_f32_e32 v170, v170
	s_nop 0
	v_add_f32_e32 v170, 1.0, v170
	v_rcp_f32_e32 v170, v170
	s_nop 0
	v_fmac_f32_e32 v153, v170, v182
	s_nop 1
	v_add_f32_dpp v153, v153, v153 quad_perm:[1,0,3,2] row_mask:0xf bank_mask:0xf bound_ctrl:1
	s_nop 1
	v_add_f32_dpp v153, v153, v153 quad_perm:[2,3,0,1] row_mask:0xf bank_mask:0xf bound_ctrl:1
	s_nop 1
	v_add_f32_dpp v153, v153, v153 row_half_mirror row_mask:0xf bank_mask:0xf bound_ctrl:1
	v_cvt_f16_f32_e32 v170, v153
	ds_write_b16 v150, v170
	s_waitcnt lgkmcnt(0)
	s_barrier
	ds_read_b128 v[154:157], v147
	s_waitcnt lgkmcnt(0)
	v_smfmac_f32_16x16x64_f16 v[130:133], v[154:157], v[248:255], v191
	s_nop 2
	v_add_u32_e32 v134, s3, v151
	ds_read_b32 v135, v134
	s_nop 2
	v_cndmask_b32_e64 v136, v130, v131, s[0:1]
	v_exp_f32_e64 v158, -|v136|
	v_max_f32 v159, 0, v136
	v_add_f32 v158, 1.0, v158
	v_log_f32 v158, v158
	s_nop 0
	v_fma_mixlo_f16 v137, v158, 1.0, v159
	ds_write_b16 v148, v137
	v_mov_b32_e32 v192, v106
	v_mov_b32_e32 v193, v110
	v_add_f32_e32 v136, v152, v153
	v_mul_f32 v137, -2.0, v135
	s_nop 5
	ds_read_b128 v[208:211], v139
	s_waitcnt lgkmcnt(1)
	s_barrier
	ds_read_b128 v[212:215], v140
	s_waitcnt lgkmcnt(1)
	v_smfmac_f32_16x16x64_f16 v[192:195], v[208:211], v[6:13], v191
	ds_read_b128 v[216:219], v141
	s_waitcnt lgkmcnt(1)
	v_smfmac_f32_16x16x64_f16 v[192:195], v[212:215], v[14:21], v191
	ds_read_b128 v[220:223], v142
	s_waitcnt lgkmcnt(1)
	v_smfmac_f32_16x16x64_f16 v[192:195], v[216:219], v[26:33], v191
	s_waitcnt lgkmcnt(0)
	v_smfmac_f32_16x16x64_f16 v[192:195], v[220:223], v[34:41], v191
	s_nop 7
	v_cndmask_b32_e64 v152, v192, v193, s[0:1]
	v_exp_f32_e64 v158, -|v152|
	v_max_f32 v159, 0, v152
	v_add_f32 v158, 1.0, v158
	v_log_f32 v158, v158
	s_nop 0
	v_fma_mixlo_f16 v153, v158, 1.0, v159
	ds_write_b16 v149, v153
	v_mov_b32_e32 v200, v114
	v_mov_b32_e32 v201, v118
	v_mov_b32_e32 v204, v122
	v_mov_b32_e32 v205, v126
	s_nop 5
	ds_read_b128 v[208:211], v143
	s_waitcnt lgkmcnt(1)
	s_barrier
	ds_read_b128 v[212:215], v144
	s_waitcnt lgkmcnt(1)
	v_smfmac_f32_16x16x64_f16 v[200:203], v[208:211], v[42:49], v191
	ds_read_b128 v[216:219], v145
	v_smfmac_f32_16x16x64_f16 v[204:207], v[208:211], v[74:81], v191
	ds_read_b128 v[220:223], v146
	s_waitcnt lgkmcnt(2)
	v_smfmac_f32_16x16x64_f16 v[200:203], v[212:215], v[50:57], v191
	v_smfmac_f32_16x16x64_f16 v[204:207], v[212:215], v[82:89], v191
	s_waitcnt lgkmcnt(1)
	v_smfmac_f32_16x16x64_f16 v[200:203], v[216:219], v[58:65], v191
	v_smfmac_f32_16x16x64_f16 v[204:207], v[216:219], v[90:97], v191
	s_waitcnt lgkmcnt(0)
	v_smfmac_f32_16x16x64_f16 v[200:203], v[220:223], v[66:73], v191
	v_smfmac_f32_16x16x64_f16 v[204:207], v[220:223], v[98:105], v191
	s_nop 6
	v_cndmask_b32_e64 v152, v201, v200, s[6:7]
	v_cndmask_b32_e64 v152, v152, v204, s[0:1]
	v_cndmask_b32_e64 v152, v152, v205, s[4:5]
	v_exp_f32_e32 v152, v152
	s_nop 0
	v_add_f32_e32 v152, 1.0, v152
	v_rcp_f32_e32 v152, v152
	s_nop 0
	v_fmac_f32_e32 v135, v152, v137
	s_nop 1
	v_add_f32_dpp v135, v135, v135 quad_perm:[1,0,3,2] row_mask:0xf bank_mask:0xf bound_ctrl:1
	s_nop 1
	v_add_f32_dpp v135, v135, v135 quad_perm:[2,3,0,1] row_mask:0xf bank_mask:0xf bound_ctrl:1
	s_nop 1
	v_add_f32_dpp v135, v135, v135 row_half_mirror row_mask:0xf bank_mask:0xf bound_ctrl:1
	v_cvt_f16_f32_e32 v137, v135
	ds_write_b16 v150, v137
	s_waitcnt lgkmcnt(0)
	s_barrier
	ds_read_b128 v[158:161], v147
	ds_read_b32 v137, v134 offset:32
	v_add_f32_e32 v135, v136, v135
	s_waitcnt lgkmcnt(1)
	v_smfmac_f32_16x16x64_f16 v[130:133], v[158:161], v[248:255], v191
	s_nop 7
	v_cndmask_b32_e64 v156, v130, v131, s[0:1]
	v_exp_f32_e64 v158, -|v156|
	v_max_f32 v159, 0, v156
	v_add_f32 v158, 1.0, v158
	v_log_f32 v158, v158
	s_nop 0
	v_fma_mixlo_f16 v157, v158, 1.0, v159
	ds_write_b16 v148, v157
	v_mov_b32_e32 v192, v106
	v_mov_b32_e32 v193, v110
	v_mul_f32 v136, -2.0, v137
	s_nop 5
	ds_read_b128 v[208:211], v139
	s_waitcnt lgkmcnt(1)
	s_barrier
	ds_read_b128 v[212:215], v140
	s_waitcnt lgkmcnt(1)
	v_smfmac_f32_16x16x64_f16 v[192:195], v[208:211], v[6:13], v191
	ds_read_b128 v[216:219], v141
	s_waitcnt lgkmcnt(1)
	v_smfmac_f32_16x16x64_f16 v[192:195], v[212:215], v[14:21], v191
	ds_read_b128 v[220:223], v142
	s_waitcnt lgkmcnt(1)
	v_smfmac_f32_16x16x64_f16 v[192:195], v[216:219], v[26:33], v191
	s_waitcnt lgkmcnt(0)
	v_smfmac_f32_16x16x64_f16 v[192:195], v[220:223], v[34:41], v191
	s_nop 7
	v_cndmask_b32_e64 v156, v192, v193, s[0:1]
	v_exp_f32_e64 v158, -|v156|
	v_max_f32 v159, 0, v156
	v_add_f32 v158, 1.0, v158
	v_log_f32 v158, v158
	s_nop 0
	v_fma_mixlo_f16 v157, v158, 1.0, v159
	ds_write_b16 v149, v157
	v_mov_b32_e32 v200, v114
	v_mov_b32_e32 v201, v118
	v_mov_b32_e32 v204, v122
	v_mov_b32_e32 v205, v126
	s_nop 5
	ds_read_b128 v[208:211], v143
	s_waitcnt lgkmcnt(1)
	s_barrier
	ds_read_b128 v[212:215], v144
	s_waitcnt lgkmcnt(1)
	v_smfmac_f32_16x16x64_f16 v[200:203], v[208:211], v[42:49], v191
	ds_read_b128 v[216:219], v145
	v_smfmac_f32_16x16x64_f16 v[204:207], v[208:211], v[74:81], v191
	ds_read_b128 v[220:223], v146
	s_waitcnt lgkmcnt(2)
	v_smfmac_f32_16x16x64_f16 v[200:203], v[212:215], v[50:57], v191
	v_smfmac_f32_16x16x64_f16 v[204:207], v[212:215], v[82:89], v191
	s_waitcnt lgkmcnt(1)
	v_smfmac_f32_16x16x64_f16 v[200:203], v[216:219], v[58:65], v191
	v_smfmac_f32_16x16x64_f16 v[204:207], v[216:219], v[90:97], v191
	s_waitcnt lgkmcnt(0)
	v_smfmac_f32_16x16x64_f16 v[200:203], v[220:223], v[66:73], v191
	v_smfmac_f32_16x16x64_f16 v[204:207], v[220:223], v[98:105], v191
	s_nop 6
	v_cndmask_b32_e64 v172, v201, v200, s[6:7]
	v_cndmask_b32_e64 v172, v172, v204, s[0:1]
	v_cndmask_b32_e64 v172, v172, v205, s[4:5]
	v_exp_f32_e32 v172, v172
	s_nop 0
	v_add_f32_e32 v172, 1.0, v172
	v_rcp_f32_e32 v172, v172
	s_nop 0
	v_fmac_f32_e32 v137, v172, v136
	s_nop 1
	v_add_f32_dpp v136, v137, v137 quad_perm:[1,0,3,2] row_mask:0xf bank_mask:0xf bound_ctrl:1
	s_nop 1
	v_add_f32_dpp v136, v136, v136 quad_perm:[2,3,0,1] row_mask:0xf bank_mask:0xf bound_ctrl:1
	s_nop 1
	v_add_f32_dpp v136, v136, v136 row_half_mirror row_mask:0xf bank_mask:0xf bound_ctrl:1
	v_cvt_f16_f32_e32 v137, v136
	ds_write_b16 v150, v137
	s_waitcnt lgkmcnt(0)
	s_barrier
	ds_read_b128 v[156:159], v147
	ds_read_b32 v137, v134 offset:64
	v_add_f32_e32 v135, v135, v136
	s_waitcnt lgkmcnt(1)
	v_smfmac_f32_16x16x64_f16 v[130:133], v[156:159], v[248:255], v191
	s_nop 7
	v_cndmask_b32_e64 v156, v130, v131, s[0:1]
	v_exp_f32_e64 v158, -|v156|
	v_max_f32 v159, 0, v156
	v_add_f32 v158, 1.0, v158
	v_log_f32 v158, v158
	s_nop 0
	v_fma_mixlo_f16 v157, v158, 1.0, v159
	ds_write_b16 v148, v157
	v_mov_b32_e32 v192, v106
	v_mov_b32_e32 v193, v110
	v_mul_f32 v136, -2.0, v137
	s_nop 5
	ds_read_b128 v[208:211], v139
	s_waitcnt lgkmcnt(1)
	s_barrier
	ds_read_b128 v[212:215], v140
	s_waitcnt lgkmcnt(1)
	v_smfmac_f32_16x16x64_f16 v[192:195], v[208:211], v[6:13], v191
	ds_read_b128 v[216:219], v141
	s_waitcnt lgkmcnt(1)
	v_smfmac_f32_16x16x64_f16 v[192:195], v[212:215], v[14:21], v191
	ds_read_b128 v[220:223], v142
	s_waitcnt lgkmcnt(1)
	v_smfmac_f32_16x16x64_f16 v[192:195], v[216:219], v[26:33], v191
	s_waitcnt lgkmcnt(0)
	v_smfmac_f32_16x16x64_f16 v[192:195], v[220:223], v[34:41], v191
	s_nop 7
	v_cndmask_b32_e64 v156, v192, v193, s[0:1]
	v_exp_f32_e64 v158, -|v156|
	v_max_f32 v159, 0, v156
	v_add_f32 v158, 1.0, v158
	v_log_f32 v158, v158
	s_nop 0
	v_fma_mixlo_f16 v157, v158, 1.0, v159
	ds_write_b16 v149, v157
	v_mov_b32_e32 v200, v114
	v_mov_b32_e32 v201, v118
	v_mov_b32_e32 v204, v122
	v_mov_b32_e32 v205, v126
	s_nop 5
	ds_read_b128 v[208:211], v143
	s_waitcnt lgkmcnt(1)
	s_barrier
	ds_read_b128 v[212:215], v144
	s_waitcnt lgkmcnt(1)
	v_smfmac_f32_16x16x64_f16 v[200:203], v[208:211], v[42:49], v191
	ds_read_b128 v[216:219], v145
	v_smfmac_f32_16x16x64_f16 v[204:207], v[208:211], v[74:81], v191
	ds_read_b128 v[220:223], v146
	s_waitcnt lgkmcnt(2)
	v_smfmac_f32_16x16x64_f16 v[200:203], v[212:215], v[50:57], v191
	v_smfmac_f32_16x16x64_f16 v[204:207], v[212:215], v[82:89], v191
	s_waitcnt lgkmcnt(1)
	v_smfmac_f32_16x16x64_f16 v[200:203], v[216:219], v[58:65], v191
	v_smfmac_f32_16x16x64_f16 v[204:207], v[216:219], v[90:97], v191
	s_waitcnt lgkmcnt(0)
	v_smfmac_f32_16x16x64_f16 v[200:203], v[220:223], v[66:73], v191
	v_smfmac_f32_16x16x64_f16 v[204:207], v[220:223], v[98:105], v191
	s_nop 6
	v_cndmask_b32_e64 v172, v201, v200, s[6:7]
	v_cndmask_b32_e64 v172, v172, v204, s[0:1]
	v_cndmask_b32_e64 v172, v172, v205, s[4:5]
	v_exp_f32_e32 v172, v172
	s_nop 0
	v_add_f32_e32 v172, 1.0, v172
	v_rcp_f32_e32 v172, v172
	s_nop 0
	v_fmac_f32_e32 v137, v172, v136
	s_nop 1
	v_add_f32_dpp v136, v137, v137 quad_perm:[1,0,3,2] row_mask:0xf bank_mask:0xf bound_ctrl:1
	s_nop 1
	v_add_f32_dpp v136, v136, v136 quad_perm:[2,3,0,1] row_mask:0xf bank_mask:0xf bound_ctrl:1
	s_nop 1
	v_add_f32_dpp v136, v136, v136 row_half_mirror row_mask:0xf bank_mask:0xf bound_ctrl:1
	v_cvt_f16_f32_e32 v137, v136
	ds_write_b16 v150, v137
	s_waitcnt lgkmcnt(0)
	s_barrier
	ds_read_b128 v[156:159], v147
	ds_read_b32 v137, v134 offset:96
	v_add_f32_e32 v135, v135, v136
	s_waitcnt lgkmcnt(1)
	v_smfmac_f32_16x16x64_f16 v[130:133], v[156:159], v[248:255], v191
	s_nop 7
	v_cndmask_b32_e64 v156, v130, v131, s[0:1]
	v_exp_f32_e64 v158, -|v156|
	v_max_f32 v159, 0, v156
	v_add_f32 v158, 1.0, v158
	v_log_f32 v158, v158
	s_nop 0
	v_fma_mixlo_f16 v157, v158, 1.0, v159
	ds_write_b16 v148, v157
	v_mov_b32_e32 v192, v106
	v_mov_b32_e32 v193, v110
	v_mul_f32 v136, -2.0, v137
	s_nop 5
	ds_read_b128 v[208:211], v139
	s_waitcnt lgkmcnt(1)
	s_barrier
	ds_read_b128 v[212:215], v140
	s_waitcnt lgkmcnt(1)
	v_smfmac_f32_16x16x64_f16 v[192:195], v[208:211], v[6:13], v191
	ds_read_b128 v[216:219], v141
	s_waitcnt lgkmcnt(1)
	v_smfmac_f32_16x16x64_f16 v[192:195], v[212:215], v[14:21], v191
	ds_read_b128 v[220:223], v142
	s_waitcnt lgkmcnt(1)
	v_smfmac_f32_16x16x64_f16 v[192:195], v[216:219], v[26:33], v191
	s_waitcnt lgkmcnt(0)
	v_smfmac_f32_16x16x64_f16 v[192:195], v[220:223], v[34:41], v191
	s_nop 7
	v_cndmask_b32_e64 v156, v192, v193, s[0:1]
	v_exp_f32_e64 v158, -|v156|
	v_max_f32 v159, 0, v156
	v_add_f32 v158, 1.0, v158
	v_log_f32 v158, v158
	s_nop 0
	v_fma_mixlo_f16 v157, v158, 1.0, v159
	ds_write_b16 v149, v157
	v_mov_b32_e32 v200, v114
	v_mov_b32_e32 v201, v118
	v_mov_b32_e32 v204, v122
	v_mov_b32_e32 v205, v126
	s_nop 5
	ds_read_b128 v[208:211], v143
	s_waitcnt lgkmcnt(1)
	s_barrier
	ds_read_b128 v[212:215], v144
	s_waitcnt lgkmcnt(1)
	v_smfmac_f32_16x16x64_f16 v[200:203], v[208:211], v[42:49], v191
	ds_read_b128 v[216:219], v145
	v_smfmac_f32_16x16x64_f16 v[204:207], v[208:211], v[74:81], v191
	ds_read_b128 v[220:223], v146
	s_waitcnt lgkmcnt(2)
	v_smfmac_f32_16x16x64_f16 v[200:203], v[212:215], v[50:57], v191
	v_smfmac_f32_16x16x64_f16 v[204:207], v[212:215], v[82:89], v191
	s_waitcnt lgkmcnt(1)
	v_smfmac_f32_16x16x64_f16 v[200:203], v[216:219], v[58:65], v191
	v_smfmac_f32_16x16x64_f16 v[204:207], v[216:219], v[90:97], v191
	s_waitcnt lgkmcnt(0)
	v_smfmac_f32_16x16x64_f16 v[200:203], v[220:223], v[66:73], v191
	v_smfmac_f32_16x16x64_f16 v[204:207], v[220:223], v[98:105], v191
	s_nop 6
	v_cndmask_b32_e64 v172, v201, v200, s[6:7]
	v_cndmask_b32_e64 v172, v172, v204, s[0:1]
	v_cndmask_b32_e64 v172, v172, v205, s[4:5]
	v_exp_f32_e32 v172, v172
	s_nop 0
	v_add_f32_e32 v172, 1.0, v172
	v_rcp_f32_e32 v172, v172
	s_nop 0
	v_fmac_f32_e32 v137, v172, v136
	s_nop 1
	v_add_f32_dpp v136, v137, v137 quad_perm:[1,0,3,2] row_mask:0xf bank_mask:0xf bound_ctrl:1
	s_nop 1
	v_add_f32_dpp v136, v136, v136 quad_perm:[2,3,0,1] row_mask:0xf bank_mask:0xf bound_ctrl:1
	s_nop 1
	v_add_f32_dpp v136, v136, v136 row_half_mirror row_mask:0xf bank_mask:0xf bound_ctrl:1
	v_cvt_f16_f32_e32 v137, v136
	ds_write_b16 v150, v137
	s_waitcnt lgkmcnt(0)
	s_barrier
	ds_read_b128 v[156:159], v147
	ds_read_b32 v137, v134 offset:128
	v_add_f32_e32 v135, v135, v136
	s_waitcnt lgkmcnt(1)
	v_smfmac_f32_16x16x64_f16 v[130:133], v[156:159], v[248:255], v191
	s_nop 7
	v_cndmask_b32_e64 v156, v130, v131, s[0:1]
	v_exp_f32_e64 v158, -|v156|
	v_max_f32 v159, 0, v156
	v_add_f32 v158, 1.0, v158
	v_log_f32 v158, v158
	s_nop 0
	v_fma_mixlo_f16 v157, v158, 1.0, v159
	ds_write_b16 v148, v157
	v_mov_b32_e32 v192, v106
	v_mov_b32_e32 v193, v110
	v_mul_f32 v136, -2.0, v137
	s_nop 5
	ds_read_b128 v[208:211], v139
	s_waitcnt lgkmcnt(1)
	s_barrier
	ds_read_b128 v[212:215], v140
	s_waitcnt lgkmcnt(1)
	v_smfmac_f32_16x16x64_f16 v[192:195], v[208:211], v[6:13], v191
	ds_read_b128 v[216:219], v141
	s_waitcnt lgkmcnt(1)
	v_smfmac_f32_16x16x64_f16 v[192:195], v[212:215], v[14:21], v191
	ds_read_b128 v[220:223], v142
	s_waitcnt lgkmcnt(1)
	v_smfmac_f32_16x16x64_f16 v[192:195], v[216:219], v[26:33], v191
	s_waitcnt lgkmcnt(0)
	v_smfmac_f32_16x16x64_f16 v[192:195], v[220:223], v[34:41], v191
	s_nop 7
	v_cndmask_b32_e64 v156, v192, v193, s[0:1]
	v_exp_f32_e64 v158, -|v156|
	v_max_f32 v159, 0, v156
	v_add_f32 v158, 1.0, v158
	v_log_f32 v158, v158
	s_nop 0
	v_fma_mixlo_f16 v157, v158, 1.0, v159
	ds_write_b16 v149, v157
	v_mov_b32_e32 v200, v114
	v_mov_b32_e32 v201, v118
	v_mov_b32_e32 v204, v122
	v_mov_b32_e32 v205, v126
	s_nop 5
	ds_read_b128 v[208:211], v143
	s_waitcnt lgkmcnt(1)
	s_barrier
	ds_read_b128 v[212:215], v144
	s_waitcnt lgkmcnt(1)
	v_smfmac_f32_16x16x64_f16 v[200:203], v[208:211], v[42:49], v191
	ds_read_b128 v[216:219], v145
	v_smfmac_f32_16x16x64_f16 v[204:207], v[208:211], v[74:81], v191
	ds_read_b128 v[220:223], v146
	s_waitcnt lgkmcnt(2)
	v_smfmac_f32_16x16x64_f16 v[200:203], v[212:215], v[50:57], v191
	v_smfmac_f32_16x16x64_f16 v[204:207], v[212:215], v[82:89], v191
	s_waitcnt lgkmcnt(1)
	v_smfmac_f32_16x16x64_f16 v[200:203], v[216:219], v[58:65], v191
	v_smfmac_f32_16x16x64_f16 v[204:207], v[216:219], v[90:97], v191
	s_waitcnt lgkmcnt(0)
	v_smfmac_f32_16x16x64_f16 v[200:203], v[220:223], v[66:73], v191
	v_smfmac_f32_16x16x64_f16 v[204:207], v[220:223], v[98:105], v191
	s_nop 6
	v_cndmask_b32_e64 v172, v201, v200, s[6:7]
	v_cndmask_b32_e64 v172, v172, v204, s[0:1]
	v_cndmask_b32_e64 v172, v172, v205, s[4:5]
	v_exp_f32_e32 v172, v172
	s_nop 0
	v_add_f32_e32 v172, 1.0, v172
	v_rcp_f32_e32 v172, v172
	s_nop 0
	v_fmac_f32_e32 v137, v172, v136
	s_nop 1
	v_add_f32_dpp v136, v137, v137 quad_perm:[1,0,3,2] row_mask:0xf bank_mask:0xf bound_ctrl:1
	s_nop 1
	v_add_f32_dpp v136, v136, v136 quad_perm:[2,3,0,1] row_mask:0xf bank_mask:0xf bound_ctrl:1
	s_nop 1
	v_add_f32_dpp v136, v136, v136 row_half_mirror row_mask:0xf bank_mask:0xf bound_ctrl:1
	v_cvt_f16_f32_e32 v137, v136
	ds_write_b16 v150, v137
	s_waitcnt lgkmcnt(0)
	s_barrier
	ds_read_b128 v[156:159], v147
	ds_read_b32 v137, v134 offset:160
	v_add_f32_e32 v135, v135, v136
	s_waitcnt lgkmcnt(1)
	v_smfmac_f32_16x16x64_f16 v[130:133], v[156:159], v[248:255], v191
	s_nop 7
	v_cndmask_b32_e64 v156, v130, v131, s[0:1]
	v_exp_f32_e64 v158, -|v156|
	v_max_f32 v159, 0, v156
	v_add_f32 v158, 1.0, v158
	v_log_f32 v158, v158
	s_nop 0
	v_fma_mixlo_f16 v157, v158, 1.0, v159
	ds_write_b16 v148, v157
	v_mov_b32_e32 v192, v106
	v_mov_b32_e32 v193, v110
	v_mul_f32 v136, -2.0, v137
	s_nop 5
	ds_read_b128 v[208:211], v139
	s_waitcnt lgkmcnt(1)
	s_barrier
	ds_read_b128 v[212:215], v140
	s_waitcnt lgkmcnt(1)
	v_smfmac_f32_16x16x64_f16 v[192:195], v[208:211], v[6:13], v191
	ds_read_b128 v[216:219], v141
	s_waitcnt lgkmcnt(1)
	v_smfmac_f32_16x16x64_f16 v[192:195], v[212:215], v[14:21], v191
	ds_read_b128 v[220:223], v142
	s_waitcnt lgkmcnt(1)
	v_smfmac_f32_16x16x64_f16 v[192:195], v[216:219], v[26:33], v191
	s_waitcnt lgkmcnt(0)
	v_smfmac_f32_16x16x64_f16 v[192:195], v[220:223], v[34:41], v191
	s_nop 7
	v_cndmask_b32_e64 v156, v192, v193, s[0:1]
	v_exp_f32_e64 v158, -|v156|
	v_max_f32 v159, 0, v156
	v_add_f32 v158, 1.0, v158
	v_log_f32 v158, v158
	s_nop 0
	v_fma_mixlo_f16 v157, v158, 1.0, v159
	ds_write_b16 v149, v157
	v_mov_b32_e32 v200, v114
	v_mov_b32_e32 v201, v118
	v_mov_b32_e32 v204, v122
	v_mov_b32_e32 v205, v126
	s_nop 5
	ds_read_b128 v[208:211], v143
	s_waitcnt lgkmcnt(1)
	s_barrier
	ds_read_b128 v[212:215], v144
	s_waitcnt lgkmcnt(1)
	v_smfmac_f32_16x16x64_f16 v[200:203], v[208:211], v[42:49], v191
	ds_read_b128 v[216:219], v145
	v_smfmac_f32_16x16x64_f16 v[204:207], v[208:211], v[74:81], v191
	ds_read_b128 v[220:223], v146
	s_waitcnt lgkmcnt(2)
	v_smfmac_f32_16x16x64_f16 v[200:203], v[212:215], v[50:57], v191
	v_smfmac_f32_16x16x64_f16 v[204:207], v[212:215], v[82:89], v191
	s_waitcnt lgkmcnt(1)
	v_smfmac_f32_16x16x64_f16 v[200:203], v[216:219], v[58:65], v191
	v_smfmac_f32_16x16x64_f16 v[204:207], v[216:219], v[90:97], v191
	s_waitcnt lgkmcnt(0)
	v_smfmac_f32_16x16x64_f16 v[200:203], v[220:223], v[66:73], v191
	v_smfmac_f32_16x16x64_f16 v[204:207], v[220:223], v[98:105], v191
	s_nop 6
	v_cndmask_b32_e64 v172, v201, v200, s[6:7]
	v_cndmask_b32_e64 v172, v172, v204, s[0:1]
	v_cndmask_b32_e64 v172, v172, v205, s[4:5]
	v_exp_f32_e32 v172, v172
	s_nop 0
	v_add_f32_e32 v172, 1.0, v172
	v_rcp_f32_e32 v172, v172
	s_nop 0
	v_fmac_f32_e32 v137, v172, v136
	s_nop 1
	v_add_f32_dpp v136, v137, v137 quad_perm:[1,0,3,2] row_mask:0xf bank_mask:0xf bound_ctrl:1
	s_nop 1
	v_add_f32_dpp v136, v136, v136 quad_perm:[2,3,0,1] row_mask:0xf bank_mask:0xf bound_ctrl:1
	s_nop 1
	v_add_f32_dpp v136, v136, v136 row_half_mirror row_mask:0xf bank_mask:0xf bound_ctrl:1
	v_cvt_f16_f32_e32 v137, v136
	ds_write_b16 v150, v137
	s_waitcnt lgkmcnt(0)
	s_barrier
	ds_read_b128 v[156:159], v147
	ds_read_b32 v137, v134 offset:192
	v_add_f32_e32 v135, v135, v136
	s_waitcnt lgkmcnt(1)
	v_smfmac_f32_16x16x64_f16 v[130:133], v[156:159], v[248:255], v191
	s_nop 7
	v_cndmask_b32_e64 v152, v130, v131, s[0:1]
	v_exp_f32_e64 v158, -|v152|
	v_max_f32 v159, 0, v152
	v_add_f32 v158, 1.0, v158
	v_log_f32 v158, v158
	s_nop 0
	v_fma_mixlo_f16 v153, v158, 1.0, v159
	ds_write_b16 v148, v153
	v_mov_b32_e32 v192, v106
	v_mov_b32_e32 v193, v110
	v_mul_f32 v136, -2.0, v137
	s_nop 5
	ds_read_b128 v[208:211], v139
	s_waitcnt lgkmcnt(1)
	s_barrier
	ds_read_b128 v[212:215], v140
	s_waitcnt lgkmcnt(1)
	v_smfmac_f32_16x16x64_f16 v[192:195], v[208:211], v[6:13], v191
	ds_read_b128 v[216:219], v141
	s_waitcnt lgkmcnt(1)
	v_smfmac_f32_16x16x64_f16 v[192:195], v[212:215], v[14:21], v191
	ds_read_b128 v[220:223], v142
	s_waitcnt lgkmcnt(1)
	v_smfmac_f32_16x16x64_f16 v[192:195], v[216:219], v[26:33], v191
	s_waitcnt lgkmcnt(0)
	v_smfmac_f32_16x16x64_f16 v[192:195], v[220:223], v[34:41], v191
	s_nop 7
	v_cndmask_b32_e64 v152, v192, v193, s[0:1]
	v_exp_f32_e64 v158, -|v152|
	v_max_f32 v159, 0, v152
	v_add_f32 v158, 1.0, v158
	v_log_f32 v158, v158
	s_nop 0
	v_fma_mixlo_f16 v153, v158, 1.0, v159
	ds_write_b16 v149, v153
	v_mov_b32_e32 v200, v114
	v_mov_b32_e32 v201, v118
	v_mov_b32_e32 v204, v122
	v_mov_b32_e32 v205, v126
	s_nop 5
	ds_read_b128 v[208:211], v143
	s_waitcnt lgkmcnt(1)
	s_barrier
	ds_read_b128 v[212:215], v144
	s_waitcnt lgkmcnt(1)
	v_smfmac_f32_16x16x64_f16 v[200:203], v[208:211], v[42:49], v191
	ds_read_b128 v[216:219], v145
	v_smfmac_f32_16x16x64_f16 v[204:207], v[208:211], v[74:81], v191
	ds_read_b128 v[220:223], v146
	s_waitcnt lgkmcnt(2)
	v_smfmac_f32_16x16x64_f16 v[200:203], v[212:215], v[50:57], v191
	v_smfmac_f32_16x16x64_f16 v[204:207], v[212:215], v[82:89], v191
	s_waitcnt lgkmcnt(1)
	v_smfmac_f32_16x16x64_f16 v[200:203], v[216:219], v[58:65], v191
	v_smfmac_f32_16x16x64_f16 v[204:207], v[216:219], v[90:97], v191
	s_waitcnt lgkmcnt(0)
	v_smfmac_f32_16x16x64_f16 v[200:203], v[220:223], v[66:73], v191
	v_smfmac_f32_16x16x64_f16 v[204:207], v[220:223], v[98:105], v191
	s_nop 6
	v_cndmask_b32_e64 v152, v201, v200, s[6:7]
	v_cndmask_b32_e64 v152, v152, v204, s[0:1]
	v_cndmask_b32_e64 v152, v152, v205, s[4:5]
	v_exp_f32_e32 v152, v152
	s_nop 0
	v_add_f32_e32 v152, 1.0, v152
	v_rcp_f32_e32 v152, v152
	s_nop 0
	v_fmac_f32_e32 v137, v152, v136
	s_nop 1
	v_add_f32_dpp v136, v137, v137 quad_perm:[1,0,3,2] row_mask:0xf bank_mask:0xf bound_ctrl:1
	s_nop 1
	v_add_f32_dpp v136, v136, v136 quad_perm:[2,3,0,1] row_mask:0xf bank_mask:0xf bound_ctrl:1
	s_nop 1
	v_add_f32_dpp v136, v136, v136 row_half_mirror row_mask:0xf bank_mask:0xf bound_ctrl:1
	v_cvt_f16_f32_e32 v137, v136
	ds_write_b16 v150, v137
	s_waitcnt lgkmcnt(0)
	s_barrier
	ds_read_b128 v[158:161], v147
	v_add_f32_e32 v152, v135, v136
	ds_read_b32 v153, v134 offset:224
	s_addk_i32 s3, 0x100
	s_cmpk_eq_u32 s3, 0xfa20
	s_waitcnt lgkmcnt(1)
	v_smfmac_f32_16x16x64_f16 v[130:133], v[158:161], v[248:255], v191
	s_nop 7
	v_cndmask_b32_e64 v154, v130, v131, s[0:1]
	s_cbranch_scc0 .LBB0_21
	s_and_saveexec_b64 s[0:1], vcc
	ds_write_b32 v1, v152
	s_or_b64 exec, exec, s[0:1]
	v_cmp_gt_u32_e32 vcc, 10, v0
	s_waitcnt lgkmcnt(0)
	s_barrier
	s_and_saveexec_b64 s[0:1], vcc
	s_cbranch_execz .LBB0_28
	v_lshlrev_b32_e32 v1, 2, v0
	global_load_dword v1, v1, s[12:13]
	v_mov_b32_e32 v139, 0
	v_lshl_add_u64 v[2:3], s[10:11], 0, v[138:139]
	v_lshl_add_u64 v[2:3], v[2:3], 0, 28
	s_mov_b32 s0, 0
